# BRANCH epilogue rewritten by hand: one branch on the segment, gate loads issued ahead through a 6-slot register ring with counted waits
# baseline (speedup 1.0000x reference)
.LBB0_387:
	v_lshl_add_u32 v0, s28, 8, v194
	s_lshl_b32 s28, s47, 8
	s_lshl_b32 s26, s29, 11
	v_mul_u32_u24_e32 v2, 0x1800, v0
	v_add_u32_e32 v3, s28, v197
	v_add3_u32 v2, v2, v3, s26
	s_cmp_lt_i32 s29, 2
	s_cbranch_scc0 .Lbr_seg2
	v_mov_b32_e32 v192, v2
	global_load_dwordx4 v[132:135], v192, s[14:15]
	global_load_dwordx4 v[136:139], v192, s[14:15] offset:2048
	v_add_u32_e32 v193, 0x18000, v2
	global_load_dwordx4 v[140:143], v193, s[14:15]
	global_load_dwordx4 v[144:147], v193, s[14:15] offset:2048
	v_add_u32_e32 v192, 0x30000, v2
	global_load_dwordx4 v[148:151], v192, s[14:15]
	global_load_dwordx4 v[152:155], v192, s[14:15] offset:2048
	v_add_u32_e32 v193, 0x48000, v2
	global_load_dwordx4 v[156:159], v193, s[14:15]
	global_load_dwordx4 v[160:163], v193, s[14:15] offset:2048
	v_add_u32_e32 v192, 0xc0000, v2
	global_load_dwordx4 v[176:179], v192, s[14:15]
	global_load_dwordx4 v[180:183], v192, s[14:15] offset:2048
	v_add_u32_e32 v193, 0xd8000, v2
	global_load_dwordx4 v[184:187], v193, s[14:15]
	global_load_dwordx4 v[188:191], v193, s[14:15] offset:2048
	s_waitcnt vmcnt(10)
	v_cvt_f32_ubyte0_e32 v204, v132
	v_cvt_f32_ubyte1_e32 v205, v132
	v_cvt_f32_ubyte2_e32 v206, v132
	v_cvt_f32_ubyte3_e32 v207, v132
	v_cvt_f32_ubyte0_e32 v208, v133
	v_cvt_f32_ubyte1_e32 v209, v133
	v_cvt_f32_ubyte2_e32 v210, v133
	v_cvt_f32_ubyte3_e32 v211, v133
	v_cvt_f32_ubyte0_e32 v212, v136
	v_cvt_f32_ubyte1_e32 v213, v136
	v_cvt_f32_ubyte2_e32 v214, v136
	v_cvt_f32_ubyte3_e32 v215, v136
	v_cvt_f32_ubyte0_e32 v216, v137
	v_cvt_f32_ubyte1_e32 v217, v137
	v_cvt_f32_ubyte2_e32 v218, v137
	v_cvt_f32_ubyte3_e32 v219, v137
	v_rcp_iflag_f32_e32 v212, v212
	v_rcp_iflag_f32_e32 v213, v213
	v_rcp_iflag_f32_e32 v214, v214
	v_rcp_iflag_f32_e32 v215, v215
	v_rcp_iflag_f32_e32 v216, v216
	v_rcp_iflag_f32_e32 v217, v217
	v_rcp_iflag_f32_e32 v218, v218
	v_rcp_iflag_f32_e32 v219, v219
	v_pk_mul_f32 v[204:205], v[212:213], v[204:205]
	v_pk_mul_f32 v[206:207], v[214:215], v[206:207]
	v_pk_mul_f32 v[208:209], v[216:217], v[208:209]
	v_pk_mul_f32 v[210:211], v[218:219], v[210:211]
	v_pk_mul_f32 v[128:129], v[128:129], v[204:205]
	v_pk_mul_f32 v[130:131], v[130:131], v[206:207]
	v_pk_mul_f32 v[124:125], v[124:125], v[208:209]
	v_pk_mul_f32 v[126:127], v[126:127], v[210:211]
	v_cvt_f32_ubyte0_e32 v204, v134
	v_cvt_f32_ubyte1_e32 v205, v134
	v_cvt_f32_ubyte2_e32 v206, v134
	v_cvt_f32_ubyte3_e32 v207, v134
	v_cvt_f32_ubyte0_e32 v208, v135
	v_cvt_f32_ubyte1_e32 v209, v135
	v_cvt_f32_ubyte2_e32 v210, v135
	v_cvt_f32_ubyte3_e32 v211, v135
	v_cvt_f32_ubyte0_e32 v212, v138
	v_cvt_f32_ubyte1_e32 v213, v138
	v_cvt_f32_ubyte2_e32 v214, v138
	v_cvt_f32_ubyte3_e32 v215, v138
	v_cvt_f32_ubyte0_e32 v216, v139
	v_cvt_f32_ubyte1_e32 v217, v139
	v_cvt_f32_ubyte2_e32 v218, v139
	v_cvt_f32_ubyte3_e32 v219, v139
	v_rcp_iflag_f32_e32 v212, v212
	v_rcp_iflag_f32_e32 v213, v213
	v_rcp_iflag_f32_e32 v214, v214
	v_rcp_iflag_f32_e32 v215, v215
	v_rcp_iflag_f32_e32 v216, v216
	v_rcp_iflag_f32_e32 v217, v217
	v_rcp_iflag_f32_e32 v218, v218
	v_rcp_iflag_f32_e32 v219, v219
	v_pk_mul_f32 v[204:205], v[212:213], v[204:205]
	v_pk_mul_f32 v[206:207], v[214:215], v[206:207]
	v_pk_mul_f32 v[208:209], v[216:217], v[208:209]
	v_pk_mul_f32 v[210:211], v[218:219], v[210:211]
	v_pk_mul_f32 v[96:97], v[96:97], v[204:205]
	v_pk_mul_f32 v[98:99], v[98:99], v[206:207]
	v_pk_mul_f32 v[92:93], v[92:93], v[208:209]
	v_pk_mul_f32 v[94:95], v[94:95], v[210:211]
	v_add_u32_e32 v192, 0xf0000, v2
	global_load_dwordx4 v[132:135], v192, s[14:15]
	global_load_dwordx4 v[136:139], v192, s[14:15] offset:2048
	s_waitcnt vmcnt(10)
	v_cvt_f32_ubyte0_e32 v204, v140
	v_cvt_f32_ubyte1_e32 v205, v140
	v_cvt_f32_ubyte2_e32 v206, v140
	v_cvt_f32_ubyte3_e32 v207, v140
	v_cvt_f32_ubyte0_e32 v208, v141
	v_cvt_f32_ubyte1_e32 v209, v141
	v_cvt_f32_ubyte2_e32 v210, v141
	v_cvt_f32_ubyte3_e32 v211, v141
	v_cvt_f32_ubyte0_e32 v212, v144
	v_cvt_f32_ubyte1_e32 v213, v144
	v_cvt_f32_ubyte2_e32 v214, v144
	v_cvt_f32_ubyte3_e32 v215, v144
	v_cvt_f32_ubyte0_e32 v216, v145
	v_cvt_f32_ubyte1_e32 v217, v145
	v_cvt_f32_ubyte2_e32 v218, v145
	v_cvt_f32_ubyte3_e32 v219, v145
	v_rcp_iflag_f32_e32 v212, v212
	v_rcp_iflag_f32_e32 v213, v213
	v_rcp_iflag_f32_e32 v214, v214
	v_rcp_iflag_f32_e32 v215, v215
	v_rcp_iflag_f32_e32 v216, v216
	v_rcp_iflag_f32_e32 v217, v217
	v_rcp_iflag_f32_e32 v218, v218
	v_rcp_iflag_f32_e32 v219, v219
	v_pk_mul_f32 v[204:205], v[212:213], v[204:205]
	v_pk_mul_f32 v[206:207], v[214:215], v[206:207]
	v_pk_mul_f32 v[208:209], v[216:217], v[208:209]
	v_pk_mul_f32 v[210:211], v[218:219], v[210:211]
	v_pk_mul_f32 v[120:121], v[120:121], v[204:205]
	v_pk_mul_f32 v[122:123], v[122:123], v[206:207]
	v_pk_mul_f32 v[116:117], v[116:117], v[208:209]
	v_pk_mul_f32 v[118:119], v[118:119], v[210:211]
	v_cvt_f32_ubyte0_e32 v204, v142
	v_cvt_f32_ubyte1_e32 v205, v142
	v_cvt_f32_ubyte2_e32 v206, v142
	v_cvt_f32_ubyte3_e32 v207, v142
	v_cvt_f32_ubyte0_e32 v208, v143
	v_cvt_f32_ubyte1_e32 v209, v143
	v_cvt_f32_ubyte2_e32 v210, v143
	v_cvt_f32_ubyte3_e32 v211, v143
	v_cvt_f32_ubyte0_e32 v212, v146
	v_cvt_f32_ubyte1_e32 v213, v146
	v_cvt_f32_ubyte2_e32 v214, v146
	v_cvt_f32_ubyte3_e32 v215, v146
	v_cvt_f32_ubyte0_e32 v216, v147
	v_cvt_f32_ubyte1_e32 v217, v147
	v_cvt_f32_ubyte2_e32 v218, v147
	v_cvt_f32_ubyte3_e32 v219, v147
	v_rcp_iflag_f32_e32 v212, v212
	v_rcp_iflag_f32_e32 v213, v213
	v_rcp_iflag_f32_e32 v214, v214
	v_rcp_iflag_f32_e32 v215, v215
	v_rcp_iflag_f32_e32 v216, v216
	v_rcp_iflag_f32_e32 v217, v217
	v_rcp_iflag_f32_e32 v218, v218
	v_rcp_iflag_f32_e32 v219, v219
	v_pk_mul_f32 v[204:205], v[212:213], v[204:205]
	v_pk_mul_f32 v[206:207], v[214:215], v[206:207]
	v_pk_mul_f32 v[208:209], v[216:217], v[208:209]
	v_pk_mul_f32 v[210:211], v[218:219], v[210:211]
	v_pk_mul_f32 v[88:89], v[88:89], v[204:205]
	v_pk_mul_f32 v[90:91], v[90:91], v[206:207]
	v_pk_mul_f32 v[84:85], v[84:85], v[208:209]
	v_pk_mul_f32 v[86:87], v[86:87], v[210:211]
	v_add_u32_e32 v193, 0x108000, v2
	global_load_dwordx4 v[140:143], v193, s[14:15]
	global_load_dwordx4 v[144:147], v193, s[14:15] offset:2048
	s_waitcnt vmcnt(10)
	v_cvt_f32_ubyte0_e32 v204, v148
	v_cvt_f32_ubyte1_e32 v205, v148
	v_cvt_f32_ubyte2_e32 v206, v148
	v_cvt_f32_ubyte3_e32 v207, v148
	v_cvt_f32_ubyte0_e32 v208, v149
	v_cvt_f32_ubyte1_e32 v209, v149
	v_cvt_f32_ubyte2_e32 v210, v149
	v_cvt_f32_ubyte3_e32 v211, v149
	v_cvt_f32_ubyte0_e32 v212, v152
	v_cvt_f32_ubyte1_e32 v213, v152
	v_cvt_f32_ubyte2_e32 v214, v152
	v_cvt_f32_ubyte3_e32 v215, v152
	v_cvt_f32_ubyte0_e32 v216, v153
	v_cvt_f32_ubyte1_e32 v217, v153
	v_cvt_f32_ubyte2_e32 v218, v153
	v_cvt_f32_ubyte3_e32 v219, v153
	v_rcp_iflag_f32_e32 v212, v212
	v_rcp_iflag_f32_e32 v213, v213
	v_rcp_iflag_f32_e32 v214, v214
	v_rcp_iflag_f32_e32 v215, v215
	v_rcp_iflag_f32_e32 v216, v216
	v_rcp_iflag_f32_e32 v217, v217
	v_rcp_iflag_f32_e32 v218, v218
	v_rcp_iflag_f32_e32 v219, v219
	v_pk_mul_f32 v[204:205], v[212:213], v[204:205]
	v_pk_mul_f32 v[206:207], v[214:215], v[206:207]
	v_pk_mul_f32 v[208:209], v[216:217], v[208:209]
	v_pk_mul_f32 v[210:211], v[218:219], v[210:211]
	v_pk_mul_f32 v[112:113], v[112:113], v[204:205]
	v_pk_mul_f32 v[114:115], v[114:115], v[206:207]
	v_pk_mul_f32 v[108:109], v[108:109], v[208:209]
	v_pk_mul_f32 v[110:111], v[110:111], v[210:211]
	v_cvt_f32_ubyte0_e32 v204, v150
	v_cvt_f32_ubyte1_e32 v205, v150
	v_cvt_f32_ubyte2_e32 v206, v150
	v_cvt_f32_ubyte3_e32 v207, v150
	v_cvt_f32_ubyte0_e32 v208, v151
	v_cvt_f32_ubyte1_e32 v209, v151
	v_cvt_f32_ubyte2_e32 v210, v151
	v_cvt_f32_ubyte3_e32 v211, v151
	v_cvt_f32_ubyte0_e32 v212, v154
	v_cvt_f32_ubyte1_e32 v213, v154
	v_cvt_f32_ubyte2_e32 v214, v154
	v_cvt_f32_ubyte3_e32 v215, v154
	v_cvt_f32_ubyte0_e32 v216, v155
	v_cvt_f32_ubyte1_e32 v217, v155
	v_cvt_f32_ubyte2_e32 v218, v155
	v_cvt_f32_ubyte3_e32 v219, v155
	v_rcp_iflag_f32_e32 v212, v212
	v_rcp_iflag_f32_e32 v213, v213
	v_rcp_iflag_f32_e32 v214, v214
	v_rcp_iflag_f32_e32 v215, v215
	v_rcp_iflag_f32_e32 v216, v216
	v_rcp_iflag_f32_e32 v217, v217
	v_rcp_iflag_f32_e32 v218, v218
	v_rcp_iflag_f32_e32 v219, v219
	v_pk_mul_f32 v[204:205], v[212:213], v[204:205]
	v_pk_mul_f32 v[206:207], v[214:215], v[206:207]
	v_pk_mul_f32 v[208:209], v[216:217], v[208:209]
	v_pk_mul_f32 v[210:211], v[218:219], v[210:211]
	v_pk_mul_f32 v[80:81], v[80:81], v[204:205]
	v_pk_mul_f32 v[82:83], v[82:83], v[206:207]
	v_pk_mul_f32 v[76:77], v[76:77], v[208:209]
	v_pk_mul_f32 v[78:79], v[78:79], v[210:211]
	s_waitcnt vmcnt(8)
	v_cvt_f32_ubyte0_e32 v204, v156
	v_cvt_f32_ubyte1_e32 v205, v156
	v_cvt_f32_ubyte2_e32 v206, v156
	v_cvt_f32_ubyte3_e32 v207, v156
	v_cvt_f32_ubyte0_e32 v208, v157
	v_cvt_f32_ubyte1_e32 v209, v157
	v_cvt_f32_ubyte2_e32 v210, v157
	v_cvt_f32_ubyte3_e32 v211, v157
	v_cvt_f32_ubyte0_e32 v212, v160
	v_cvt_f32_ubyte1_e32 v213, v160
	v_cvt_f32_ubyte2_e32 v214, v160
	v_cvt_f32_ubyte3_e32 v215, v160
	v_cvt_f32_ubyte0_e32 v216, v161
	v_cvt_f32_ubyte1_e32 v217, v161
	v_cvt_f32_ubyte2_e32 v218, v161
	v_cvt_f32_ubyte3_e32 v219, v161
	v_rcp_iflag_f32_e32 v212, v212
	v_rcp_iflag_f32_e32 v213, v213
	v_rcp_iflag_f32_e32 v214, v214
	v_rcp_iflag_f32_e32 v215, v215
	v_rcp_iflag_f32_e32 v216, v216
	v_rcp_iflag_f32_e32 v217, v217
	v_rcp_iflag_f32_e32 v218, v218
	v_rcp_iflag_f32_e32 v219, v219
	v_pk_mul_f32 v[204:205], v[212:213], v[204:205]
	v_pk_mul_f32 v[206:207], v[214:215], v[206:207]
	v_pk_mul_f32 v[208:209], v[216:217], v[208:209]
	v_pk_mul_f32 v[210:211], v[218:219], v[210:211]
	v_pk_mul_f32 v[104:105], v[104:105], v[204:205]
	v_pk_mul_f32 v[106:107], v[106:107], v[206:207]
	v_pk_mul_f32 v[100:101], v[100:101], v[208:209]
	v_pk_mul_f32 v[102:103], v[102:103], v[210:211]
	v_cvt_f32_ubyte0_e32 v204, v158
	v_cvt_f32_ubyte1_e32 v205, v158
	v_cvt_f32_ubyte2_e32 v206, v158
	v_cvt_f32_ubyte3_e32 v207, v158
	v_cvt_f32_ubyte0_e32 v208, v159
	v_cvt_f32_ubyte1_e32 v209, v159
	v_cvt_f32_ubyte2_e32 v210, v159
	v_cvt_f32_ubyte3_e32 v211, v159
	v_cvt_f32_ubyte0_e32 v212, v162
	v_cvt_f32_ubyte1_e32 v213, v162
	v_cvt_f32_ubyte2_e32 v214, v162
	v_cvt_f32_ubyte3_e32 v215, v162
	v_cvt_f32_ubyte0_e32 v216, v163
	v_cvt_f32_ubyte1_e32 v217, v163
	v_cvt_f32_ubyte2_e32 v218, v163
	v_cvt_f32_ubyte3_e32 v219, v163
	v_rcp_iflag_f32_e32 v212, v212
	v_rcp_iflag_f32_e32 v213, v213
	v_rcp_iflag_f32_e32 v214, v214
	v_rcp_iflag_f32_e32 v215, v215
	v_rcp_iflag_f32_e32 v216, v216
	v_rcp_iflag_f32_e32 v217, v217
	v_rcp_iflag_f32_e32 v218, v218
	v_rcp_iflag_f32_e32 v219, v219
	v_pk_mul_f32 v[204:205], v[212:213], v[204:205]
	v_pk_mul_f32 v[206:207], v[214:215], v[206:207]
	v_pk_mul_f32 v[208:209], v[216:217], v[208:209]
	v_pk_mul_f32 v[210:211], v[218:219], v[210:211]
	v_pk_mul_f32 v[72:73], v[72:73], v[204:205]
	v_pk_mul_f32 v[74:75], v[74:75], v[206:207]
	v_pk_mul_f32 v[68:69], v[68:69], v[208:209]
	v_pk_mul_f32 v[70:71], v[70:71], v[210:211]
	s_waitcnt vmcnt(6)
	v_cvt_f32_ubyte0_e32 v204, v176
	v_cvt_f32_ubyte1_e32 v205, v176
	v_cvt_f32_ubyte2_e32 v206, v176
	v_cvt_f32_ubyte3_e32 v207, v176
	v_cvt_f32_ubyte0_e32 v208, v177
	v_cvt_f32_ubyte1_e32 v209, v177
	v_cvt_f32_ubyte2_e32 v210, v177
	v_cvt_f32_ubyte3_e32 v211, v177
	v_cvt_f32_ubyte0_e32 v212, v180
	v_cvt_f32_ubyte1_e32 v213, v180
	v_cvt_f32_ubyte2_e32 v214, v180
	v_cvt_f32_ubyte3_e32 v215, v180
	v_cvt_f32_ubyte0_e32 v216, v181
	v_cvt_f32_ubyte1_e32 v217, v181
	v_cvt_f32_ubyte2_e32 v218, v181
	v_cvt_f32_ubyte3_e32 v219, v181
	v_rcp_iflag_f32_e32 v212, v212
	v_rcp_iflag_f32_e32 v213, v213
	v_rcp_iflag_f32_e32 v214, v214
	v_rcp_iflag_f32_e32 v215, v215
	v_rcp_iflag_f32_e32 v216, v216
	v_rcp_iflag_f32_e32 v217, v217
	v_rcp_iflag_f32_e32 v218, v218
	v_rcp_iflag_f32_e32 v219, v219
	v_pk_mul_f32 v[204:205], v[212:213], v[204:205]
	v_pk_mul_f32 v[206:207], v[214:215], v[206:207]
	v_pk_mul_f32 v[208:209], v[216:217], v[208:209]
	v_pk_mul_f32 v[210:211], v[218:219], v[210:211]
	v_pk_mul_f32 v[64:65], v[64:65], v[204:205]
	v_pk_mul_f32 v[66:67], v[66:67], v[206:207]
	v_pk_mul_f32 v[60:61], v[60:61], v[208:209]
	v_pk_mul_f32 v[62:63], v[62:63], v[210:211]
	v_cvt_f32_ubyte0_e32 v204, v178
	v_cvt_f32_ubyte1_e32 v205, v178
	v_cvt_f32_ubyte2_e32 v206, v178
	v_cvt_f32_ubyte3_e32 v207, v178
	v_cvt_f32_ubyte0_e32 v208, v179
	v_cvt_f32_ubyte1_e32 v209, v179
	v_cvt_f32_ubyte2_e32 v210, v179
	v_cvt_f32_ubyte3_e32 v211, v179
	v_cvt_f32_ubyte0_e32 v212, v182
	v_cvt_f32_ubyte1_e32 v213, v182
	v_cvt_f32_ubyte2_e32 v214, v182
	v_cvt_f32_ubyte3_e32 v215, v182
	v_cvt_f32_ubyte0_e32 v216, v183
	v_cvt_f32_ubyte1_e32 v217, v183
	v_cvt_f32_ubyte2_e32 v218, v183
	v_cvt_f32_ubyte3_e32 v219, v183
	v_rcp_iflag_f32_e32 v212, v212
	v_rcp_iflag_f32_e32 v213, v213
	v_rcp_iflag_f32_e32 v214, v214
	v_rcp_iflag_f32_e32 v215, v215
	v_rcp_iflag_f32_e32 v216, v216
	v_rcp_iflag_f32_e32 v217, v217
	v_rcp_iflag_f32_e32 v218, v218
	v_rcp_iflag_f32_e32 v219, v219
	v_pk_mul_f32 v[204:205], v[212:213], v[204:205]
	v_pk_mul_f32 v[206:207], v[214:215], v[206:207]
	v_pk_mul_f32 v[208:209], v[216:217], v[208:209]
	v_pk_mul_f32 v[210:211], v[218:219], v[210:211]
	v_pk_mul_f32 v[32:33], v[32:33], v[204:205]
	v_pk_mul_f32 v[34:35], v[34:35], v[206:207]
	v_pk_mul_f32 v[28:29], v[28:29], v[208:209]
	v_pk_mul_f32 v[30:31], v[30:31], v[210:211]
	s_waitcnt vmcnt(4)
	v_cvt_f32_ubyte0_e32 v204, v184
	v_cvt_f32_ubyte1_e32 v205, v184
	v_cvt_f32_ubyte2_e32 v206, v184
	v_cvt_f32_ubyte3_e32 v207, v184
	v_cvt_f32_ubyte0_e32 v208, v185
	v_cvt_f32_ubyte1_e32 v209, v185
	v_cvt_f32_ubyte2_e32 v210, v185
	v_cvt_f32_ubyte3_e32 v211, v185
	v_cvt_f32_ubyte0_e32 v212, v188
	v_cvt_f32_ubyte1_e32 v213, v188
	v_cvt_f32_ubyte2_e32 v214, v188
	v_cvt_f32_ubyte3_e32 v215, v188
	v_cvt_f32_ubyte0_e32 v216, v189
	v_cvt_f32_ubyte1_e32 v217, v189
	v_cvt_f32_ubyte2_e32 v218, v189
	v_cvt_f32_ubyte3_e32 v219, v189
	v_rcp_iflag_f32_e32 v212, v212
	v_rcp_iflag_f32_e32 v213, v213
	v_rcp_iflag_f32_e32 v214, v214
	v_rcp_iflag_f32_e32 v215, v215
	v_rcp_iflag_f32_e32 v216, v216
	v_rcp_iflag_f32_e32 v217, v217
	v_rcp_iflag_f32_e32 v218, v218
	v_rcp_iflag_f32_e32 v219, v219
	v_pk_mul_f32 v[204:205], v[212:213], v[204:205]
	v_pk_mul_f32 v[206:207], v[214:215], v[206:207]
	v_pk_mul_f32 v[208:209], v[216:217], v[208:209]
	v_pk_mul_f32 v[210:211], v[218:219], v[210:211]
	v_pk_mul_f32 v[56:57], v[56:57], v[204:205]
	v_pk_mul_f32 v[58:59], v[58:59], v[206:207]
	v_pk_mul_f32 v[52:53], v[52:53], v[208:209]
	v_pk_mul_f32 v[54:55], v[54:55], v[210:211]
	v_cvt_f32_ubyte0_e32 v204, v186
	v_cvt_f32_ubyte1_e32 v205, v186
	v_cvt_f32_ubyte2_e32 v206, v186
	v_cvt_f32_ubyte3_e32 v207, v186
	v_cvt_f32_ubyte0_e32 v208, v187
	v_cvt_f32_ubyte1_e32 v209, v187
	v_cvt_f32_ubyte2_e32 v210, v187
	v_cvt_f32_ubyte3_e32 v211, v187
	v_cvt_f32_ubyte0_e32 v212, v190
	v_cvt_f32_ubyte1_e32 v213, v190
	v_cvt_f32_ubyte2_e32 v214, v190
	v_cvt_f32_ubyte3_e32 v215, v190
	v_cvt_f32_ubyte0_e32 v216, v191
	v_cvt_f32_ubyte1_e32 v217, v191
	v_cvt_f32_ubyte2_e32 v218, v191
	v_cvt_f32_ubyte3_e32 v219, v191
	v_rcp_iflag_f32_e32 v212, v212
	v_rcp_iflag_f32_e32 v213, v213
	v_rcp_iflag_f32_e32 v214, v214
	v_rcp_iflag_f32_e32 v215, v215
	v_rcp_iflag_f32_e32 v216, v216
	v_rcp_iflag_f32_e32 v217, v217
	v_rcp_iflag_f32_e32 v218, v218
	v_rcp_iflag_f32_e32 v219, v219
	v_pk_mul_f32 v[204:205], v[212:213], v[204:205]
	v_pk_mul_f32 v[206:207], v[214:215], v[206:207]
	v_pk_mul_f32 v[208:209], v[216:217], v[208:209]
	v_pk_mul_f32 v[210:211], v[218:219], v[210:211]
	v_pk_mul_f32 v[24:25], v[24:25], v[204:205]
	v_pk_mul_f32 v[26:27], v[26:27], v[206:207]
	v_pk_mul_f32 v[20:21], v[20:21], v[208:209]
	v_pk_mul_f32 v[22:23], v[22:23], v[210:211]
	s_waitcnt vmcnt(2)
	v_cvt_f32_ubyte0_e32 v204, v132
	v_cvt_f32_ubyte1_e32 v205, v132
	v_cvt_f32_ubyte2_e32 v206, v132
	v_cvt_f32_ubyte3_e32 v207, v132
	v_cvt_f32_ubyte0_e32 v208, v133
	v_cvt_f32_ubyte1_e32 v209, v133
	v_cvt_f32_ubyte2_e32 v210, v133
	v_cvt_f32_ubyte3_e32 v211, v133
	v_cvt_f32_ubyte0_e32 v212, v136
	v_cvt_f32_ubyte1_e32 v213, v136
	v_cvt_f32_ubyte2_e32 v214, v136
	v_cvt_f32_ubyte3_e32 v215, v136
	v_cvt_f32_ubyte0_e32 v216, v137
	v_cvt_f32_ubyte1_e32 v217, v137
	v_cvt_f32_ubyte2_e32 v218, v137
	v_cvt_f32_ubyte3_e32 v219, v137
	v_rcp_iflag_f32_e32 v212, v212
	v_rcp_iflag_f32_e32 v213, v213
	v_rcp_iflag_f32_e32 v214, v214
	v_rcp_iflag_f32_e32 v215, v215
	v_rcp_iflag_f32_e32 v216, v216
	v_rcp_iflag_f32_e32 v217, v217
	v_rcp_iflag_f32_e32 v218, v218
	v_rcp_iflag_f32_e32 v219, v219
	v_pk_mul_f32 v[204:205], v[212:213], v[204:205]
	v_pk_mul_f32 v[206:207], v[214:215], v[206:207]
	v_pk_mul_f32 v[208:209], v[216:217], v[208:209]
	v_pk_mul_f32 v[210:211], v[218:219], v[210:211]
	v_pk_mul_f32 v[48:49], v[48:49], v[204:205]
	v_pk_mul_f32 v[50:51], v[50:51], v[206:207]
	v_pk_mul_f32 v[44:45], v[44:45], v[208:209]
	v_pk_mul_f32 v[46:47], v[46:47], v[210:211]
	v_cvt_f32_ubyte0_e32 v204, v134
	v_cvt_f32_ubyte1_e32 v205, v134
	v_cvt_f32_ubyte2_e32 v206, v134
	v_cvt_f32_ubyte3_e32 v207, v134
	v_cvt_f32_ubyte0_e32 v208, v135
	v_cvt_f32_ubyte1_e32 v209, v135
	v_cvt_f32_ubyte2_e32 v210, v135
	v_cvt_f32_ubyte3_e32 v211, v135
	v_cvt_f32_ubyte0_e32 v212, v138
	v_cvt_f32_ubyte1_e32 v213, v138
	v_cvt_f32_ubyte2_e32 v214, v138
	v_cvt_f32_ubyte3_e32 v215, v138
	v_cvt_f32_ubyte0_e32 v216, v139
	v_cvt_f32_ubyte1_e32 v217, v139
	v_cvt_f32_ubyte2_e32 v218, v139
	v_cvt_f32_ubyte3_e32 v219, v139
	v_rcp_iflag_f32_e32 v212, v212
	v_rcp_iflag_f32_e32 v213, v213
	v_rcp_iflag_f32_e32 v214, v214
	v_rcp_iflag_f32_e32 v215, v215
	v_rcp_iflag_f32_e32 v216, v216
	v_rcp_iflag_f32_e32 v217, v217
	v_rcp_iflag_f32_e32 v218, v218
	v_rcp_iflag_f32_e32 v219, v219
	v_pk_mul_f32 v[204:205], v[212:213], v[204:205]
	v_pk_mul_f32 v[206:207], v[214:215], v[206:207]
	v_pk_mul_f32 v[208:209], v[216:217], v[208:209]
	v_pk_mul_f32 v[210:211], v[218:219], v[210:211]
	v_pk_mul_f32 v[16:17], v[16:17], v[204:205]
	v_pk_mul_f32 v[18:19], v[18:19], v[206:207]
	v_pk_mul_f32 v[12:13], v[12:13], v[208:209]
	v_pk_mul_f32 v[14:15], v[14:15], v[210:211]
	s_waitcnt vmcnt(0)
	v_cvt_f32_ubyte0_e32 v204, v140
	v_cvt_f32_ubyte1_e32 v205, v140
	v_cvt_f32_ubyte2_e32 v206, v140
	v_cvt_f32_ubyte3_e32 v207, v140
	v_cvt_f32_ubyte0_e32 v208, v141
	v_cvt_f32_ubyte1_e32 v209, v141
	v_cvt_f32_ubyte2_e32 v210, v141
	v_cvt_f32_ubyte3_e32 v211, v141
	v_cvt_f32_ubyte0_e32 v212, v144
	v_cvt_f32_ubyte1_e32 v213, v144
	v_cvt_f32_ubyte2_e32 v214, v144
	v_cvt_f32_ubyte3_e32 v215, v144
	v_cvt_f32_ubyte0_e32 v216, v145
	v_cvt_f32_ubyte1_e32 v217, v145
	v_cvt_f32_ubyte2_e32 v218, v145
	v_cvt_f32_ubyte3_e32 v219, v145
	v_rcp_iflag_f32_e32 v212, v212
	v_rcp_iflag_f32_e32 v213, v213
	v_rcp_iflag_f32_e32 v214, v214
	v_rcp_iflag_f32_e32 v215, v215
	v_rcp_iflag_f32_e32 v216, v216
	v_rcp_iflag_f32_e32 v217, v217
	v_rcp_iflag_f32_e32 v218, v218
	v_rcp_iflag_f32_e32 v219, v219
	v_pk_mul_f32 v[204:205], v[212:213], v[204:205]
	v_pk_mul_f32 v[206:207], v[214:215], v[206:207]
	v_pk_mul_f32 v[208:209], v[216:217], v[208:209]
	v_pk_mul_f32 v[210:211], v[218:219], v[210:211]
	v_pk_mul_f32 v[40:41], v[40:41], v[204:205]
	v_pk_mul_f32 v[42:43], v[42:43], v[206:207]
	v_pk_mul_f32 v[36:37], v[36:37], v[208:209]
	v_pk_mul_f32 v[38:39], v[38:39], v[210:211]
	v_cvt_f32_ubyte0_e32 v204, v142
	v_cvt_f32_ubyte1_e32 v205, v142
	v_cvt_f32_ubyte2_e32 v206, v142
	v_cvt_f32_ubyte3_e32 v207, v142
	v_cvt_f32_ubyte0_e32 v208, v143
	v_cvt_f32_ubyte1_e32 v209, v143
	v_cvt_f32_ubyte2_e32 v210, v143
	v_cvt_f32_ubyte3_e32 v211, v143
	v_cvt_f32_ubyte0_e32 v212, v146
	v_cvt_f32_ubyte1_e32 v213, v146
	v_cvt_f32_ubyte2_e32 v214, v146
	v_cvt_f32_ubyte3_e32 v215, v146
	v_cvt_f32_ubyte0_e32 v216, v147
	v_cvt_f32_ubyte1_e32 v217, v147
	v_cvt_f32_ubyte2_e32 v218, v147
	v_cvt_f32_ubyte3_e32 v219, v147
	v_rcp_iflag_f32_e32 v212, v212
	v_rcp_iflag_f32_e32 v213, v213
	v_rcp_iflag_f32_e32 v214, v214
	v_rcp_iflag_f32_e32 v215, v215
	v_rcp_iflag_f32_e32 v216, v216
	v_rcp_iflag_f32_e32 v217, v217
	v_rcp_iflag_f32_e32 v218, v218
	v_rcp_iflag_f32_e32 v219, v219
	v_pk_mul_f32 v[204:205], v[212:213], v[204:205]
	v_pk_mul_f32 v[206:207], v[214:215], v[206:207]
	v_pk_mul_f32 v[208:209], v[216:217], v[208:209]
	v_pk_mul_f32 v[210:211], v[218:219], v[210:211]
	v_pk_mul_f32 v[8:9], v[8:9], v[204:205]
	v_pk_mul_f32 v[10:11], v[10:11], v[206:207]
	v_pk_mul_f32 v[4:5], v[4:5], v[208:209]
	v_pk_mul_f32 v[6:7], v[6:7], v[210:211]
	s_mov_b64 s[6:7], -1
	s_branch .Lbr_done
.Lbr_seg2:
	v_add_u32_e32 v192, s28, v196
	v_lshlrev_b32_e32 v192, 1, v192
	v_lshl_add_u32 v192, v0, 12, v192
	v_mov_b32_e32 v193, v2
	global_load_dwordx4 v[132:135], v193, s[14:15]
	v_add_u32_e32 v3, 0x18000, v2
	global_load_dwordx4 v[136:139], v3, s[14:15]
	v_add_u32_e32 v193, 0x30000, v2
	global_load_dwordx4 v[140:143], v193, s[14:15]
	v_add_u32_e32 v3, 0x48000, v2
	global_load_dwordx4 v[144:147], v3, s[14:15]
	v_add_u32_e32 v193, 0xc0000, v2
	global_load_dwordx4 v[148:151], v193, s[14:15]
	v_add_u32_e32 v3, 0xd8000, v2
	global_load_dwordx4 v[152:155], v3, s[14:15]
	v_add_u32_e32 v193, 0xf0000, v2
	global_load_dwordx4 v[156:159], v193, s[14:15]
	v_add_u32_e32 v3, 0x108000, v2
	global_load_dwordx4 v[160:163], v3, s[14:15]
	s_waitcnt vmcnt(7)
	v_mov_b32_e32 v193, v192
	v_cvt_f32_ubyte0_e32 v204, v132
	v_cvt_f32_ubyte1_e32 v205, v132
	v_cvt_f32_ubyte2_e32 v206, v132
	v_cvt_f32_ubyte3_e32 v207, v132
	v_cvt_f32_ubyte0_e32 v208, v133
	v_cvt_f32_ubyte1_e32 v209, v133
	v_cvt_f32_ubyte2_e32 v210, v133
	v_cvt_f32_ubyte3_e32 v211, v133
	v_pk_mul_f32 v[204:205], v[204:205], s[88:89] op_sel_hi:[1,0]
	v_pk_mul_f32 v[206:207], v[206:207], s[88:89] op_sel_hi:[1,0]
	v_pk_mul_f32 v[208:209], v[208:209], s[88:89] op_sel_hi:[1,0]
	v_pk_mul_f32 v[210:211], v[210:211], s[88:89] op_sel_hi:[1,0]
	v_pk_mul_f32 v[204:205], v[128:129], v[204:205]
	v_pk_mul_f32 v[206:207], v[130:131], v[206:207]
	v_pk_mul_f32 v[208:209], v[124:125], v[208:209]
	v_pk_mul_f32 v[210:211], v[126:127], v[210:211]
	v_cvt_pk_bf16_f32 v176, v204, v205
	v_cvt_pk_bf16_f32 v177, v206, v207
	v_cvt_pk_bf16_f32 v178, v208, v209
	v_cvt_pk_bf16_f32 v179, v210, v211
	global_store_dwordx4 v193, v[176:179], s[16:17]
	v_cvt_f32_ubyte0_e32 v204, v134
	v_cvt_f32_ubyte1_e32 v205, v134
	v_cvt_f32_ubyte2_e32 v206, v134
	v_cvt_f32_ubyte3_e32 v207, v134
	v_cvt_f32_ubyte0_e32 v208, v135
	v_cvt_f32_ubyte1_e32 v209, v135
	v_cvt_f32_ubyte2_e32 v210, v135
	v_cvt_f32_ubyte3_e32 v211, v135
	v_pk_mul_f32 v[204:205], v[204:205], s[88:89] op_sel_hi:[1,0]
	v_pk_mul_f32 v[206:207], v[206:207], s[88:89] op_sel_hi:[1,0]
	v_pk_mul_f32 v[208:209], v[208:209], s[88:89] op_sel_hi:[1,0]
	v_pk_mul_f32 v[210:211], v[210:211], s[88:89] op_sel_hi:[1,0]
	v_pk_mul_f32 v[204:205], v[96:97], v[204:205]
	v_pk_mul_f32 v[206:207], v[98:99], v[206:207]
	v_pk_mul_f32 v[208:209], v[92:93], v[208:209]
	v_pk_mul_f32 v[210:211], v[94:95], v[210:211]
	v_cvt_pk_bf16_f32 v180, v204, v205
	v_cvt_pk_bf16_f32 v181, v206, v207
	v_cvt_pk_bf16_f32 v182, v208, v209
	v_cvt_pk_bf16_f32 v183, v210, v211
	global_store_dwordx4 v193, v[180:183], s[16:17] offset:256
	s_waitcnt vmcnt(8)
	v_add_u32_e32 v3, 0x10000, v192
	v_cvt_f32_ubyte0_e32 v204, v136
	v_cvt_f32_ubyte1_e32 v205, v136
	v_cvt_f32_ubyte2_e32 v206, v136
	v_cvt_f32_ubyte3_e32 v207, v136
	v_cvt_f32_ubyte0_e32 v208, v137
	v_cvt_f32_ubyte1_e32 v209, v137
	v_cvt_f32_ubyte2_e32 v210, v137
	v_cvt_f32_ubyte3_e32 v211, v137
	v_pk_mul_f32 v[204:205], v[204:205], s[88:89] op_sel_hi:[1,0]
	v_pk_mul_f32 v[206:207], v[206:207], s[88:89] op_sel_hi:[1,0]
	v_pk_mul_f32 v[208:209], v[208:209], s[88:89] op_sel_hi:[1,0]
	v_pk_mul_f32 v[210:211], v[210:211], s[88:89] op_sel_hi:[1,0]
	v_pk_mul_f32 v[204:205], v[120:121], v[204:205]
	v_pk_mul_f32 v[206:207], v[122:123], v[206:207]
	v_pk_mul_f32 v[208:209], v[116:117], v[208:209]
	v_pk_mul_f32 v[210:211], v[118:119], v[210:211]
	v_cvt_pk_bf16_f32 v184, v204, v205
	v_cvt_pk_bf16_f32 v185, v206, v207
	v_cvt_pk_bf16_f32 v186, v208, v209
	v_cvt_pk_bf16_f32 v187, v210, v211
	global_store_dwordx4 v3, v[184:187], s[16:17]
	v_cvt_f32_ubyte0_e32 v204, v138
	v_cvt_f32_ubyte1_e32 v205, v138
	v_cvt_f32_ubyte2_e32 v206, v138
	v_cvt_f32_ubyte3_e32 v207, v138
	v_cvt_f32_ubyte0_e32 v208, v139
	v_cvt_f32_ubyte1_e32 v209, v139
	v_cvt_f32_ubyte2_e32 v210, v139
	v_cvt_f32_ubyte3_e32 v211, v139
	v_pk_mul_f32 v[204:205], v[204:205], s[88:89] op_sel_hi:[1,0]
	v_pk_mul_f32 v[206:207], v[206:207], s[88:89] op_sel_hi:[1,0]
	v_pk_mul_f32 v[208:209], v[208:209], s[88:89] op_sel_hi:[1,0]
	v_pk_mul_f32 v[210:211], v[210:211], s[88:89] op_sel_hi:[1,0]
	v_pk_mul_f32 v[204:205], v[88:89], v[204:205]
	v_pk_mul_f32 v[206:207], v[90:91], v[206:207]
	v_pk_mul_f32 v[208:209], v[84:85], v[208:209]
	v_pk_mul_f32 v[210:211], v[86:87], v[210:211]
	v_cvt_pk_bf16_f32 v188, v204, v205
	v_cvt_pk_bf16_f32 v189, v206, v207
	v_cvt_pk_bf16_f32 v190, v208, v209
	v_cvt_pk_bf16_f32 v191, v210, v211
	global_store_dwordx4 v3, v[188:191], s[16:17] offset:256
	s_waitcnt vmcnt(9)
	v_add_u32_e32 v193, 0x20000, v192
	v_cvt_f32_ubyte0_e32 v204, v140
	v_cvt_f32_ubyte1_e32 v205, v140
	v_cvt_f32_ubyte2_e32 v206, v140
	v_cvt_f32_ubyte3_e32 v207, v140
	v_cvt_f32_ubyte0_e32 v208, v141
	v_cvt_f32_ubyte1_e32 v209, v141
	v_cvt_f32_ubyte2_e32 v210, v141
	v_cvt_f32_ubyte3_e32 v211, v141
	v_pk_mul_f32 v[204:205], v[204:205], s[88:89] op_sel_hi:[1,0]
	v_pk_mul_f32 v[206:207], v[206:207], s[88:89] op_sel_hi:[1,0]
	v_pk_mul_f32 v[208:209], v[208:209], s[88:89] op_sel_hi:[1,0]
	v_pk_mul_f32 v[210:211], v[210:211], s[88:89] op_sel_hi:[1,0]
	v_pk_mul_f32 v[204:205], v[112:113], v[204:205]
	v_pk_mul_f32 v[206:207], v[114:115], v[206:207]
	v_pk_mul_f32 v[208:209], v[108:109], v[208:209]
	v_pk_mul_f32 v[210:211], v[110:111], v[210:211]
	v_cvt_pk_bf16_f32 v176, v204, v205
	v_cvt_pk_bf16_f32 v177, v206, v207
	v_cvt_pk_bf16_f32 v178, v208, v209
	v_cvt_pk_bf16_f32 v179, v210, v211
	global_store_dwordx4 v193, v[176:179], s[16:17]
	v_cvt_f32_ubyte0_e32 v204, v142
	v_cvt_f32_ubyte1_e32 v205, v142
	v_cvt_f32_ubyte2_e32 v206, v142
	v_cvt_f32_ubyte3_e32 v207, v142
	v_cvt_f32_ubyte0_e32 v208, v143
	v_cvt_f32_ubyte1_e32 v209, v143
	v_cvt_f32_ubyte2_e32 v210, v143
	v_cvt_f32_ubyte3_e32 v211, v143
	v_pk_mul_f32 v[204:205], v[204:205], s[88:89] op_sel_hi:[1,0]
	v_pk_mul_f32 v[206:207], v[206:207], s[88:89] op_sel_hi:[1,0]
	v_pk_mul_f32 v[208:209], v[208:209], s[88:89] op_sel_hi:[1,0]
	v_pk_mul_f32 v[210:211], v[210:211], s[88:89] op_sel_hi:[1,0]
	v_pk_mul_f32 v[204:205], v[80:81], v[204:205]
	v_pk_mul_f32 v[206:207], v[82:83], v[206:207]
	v_pk_mul_f32 v[208:209], v[76:77], v[208:209]
	v_pk_mul_f32 v[210:211], v[78:79], v[210:211]
	v_cvt_pk_bf16_f32 v180, v204, v205
	v_cvt_pk_bf16_f32 v181, v206, v207
	v_cvt_pk_bf16_f32 v182, v208, v209
	v_cvt_pk_bf16_f32 v183, v210, v211
	global_store_dwordx4 v193, v[180:183], s[16:17] offset:256
	s_waitcnt vmcnt(10)
	v_add_u32_e32 v3, 0x30000, v192
	v_cvt_f32_ubyte0_e32 v204, v144
	v_cvt_f32_ubyte1_e32 v205, v144
	v_cvt_f32_ubyte2_e32 v206, v144
	v_cvt_f32_ubyte3_e32 v207, v144
	v_cvt_f32_ubyte0_e32 v208, v145
	v_cvt_f32_ubyte1_e32 v209, v145
	v_cvt_f32_ubyte2_e32 v210, v145
	v_cvt_f32_ubyte3_e32 v211, v145
	v_pk_mul_f32 v[204:205], v[204:205], s[88:89] op_sel_hi:[1,0]
	v_pk_mul_f32 v[206:207], v[206:207], s[88:89] op_sel_hi:[1,0]
	v_pk_mul_f32 v[208:209], v[208:209], s[88:89] op_sel_hi:[1,0]
	v_pk_mul_f32 v[210:211], v[210:211], s[88:89] op_sel_hi:[1,0]
	v_pk_mul_f32 v[204:205], v[104:105], v[204:205]
	v_pk_mul_f32 v[206:207], v[106:107], v[206:207]
	v_pk_mul_f32 v[208:209], v[100:101], v[208:209]
	v_pk_mul_f32 v[210:211], v[102:103], v[210:211]
	v_cvt_pk_bf16_f32 v184, v204, v205
	v_cvt_pk_bf16_f32 v185, v206, v207
	v_cvt_pk_bf16_f32 v186, v208, v209
	v_cvt_pk_bf16_f32 v187, v210, v211
	global_store_dwordx4 v3, v[184:187], s[16:17]
	v_cvt_f32_ubyte0_e32 v204, v146
	v_cvt_f32_ubyte1_e32 v205, v146
	v_cvt_f32_ubyte2_e32 v206, v146
	v_cvt_f32_ubyte3_e32 v207, v146
	v_cvt_f32_ubyte0_e32 v208, v147
	v_cvt_f32_ubyte1_e32 v209, v147
	v_cvt_f32_ubyte2_e32 v210, v147
	v_cvt_f32_ubyte3_e32 v211, v147
	v_pk_mul_f32 v[204:205], v[204:205], s[88:89] op_sel_hi:[1,0]
	v_pk_mul_f32 v[206:207], v[206:207], s[88:89] op_sel_hi:[1,0]
	v_pk_mul_f32 v[208:209], v[208:209], s[88:89] op_sel_hi:[1,0]
	v_pk_mul_f32 v[210:211], v[210:211], s[88:89] op_sel_hi:[1,0]
	v_pk_mul_f32 v[204:205], v[72:73], v[204:205]
	v_pk_mul_f32 v[206:207], v[74:75], v[206:207]
	v_pk_mul_f32 v[208:209], v[68:69], v[208:209]
	v_pk_mul_f32 v[210:211], v[70:71], v[210:211]
	v_cvt_pk_bf16_f32 v188, v204, v205
	v_cvt_pk_bf16_f32 v189, v206, v207
	v_cvt_pk_bf16_f32 v190, v208, v209
	v_cvt_pk_bf16_f32 v191, v210, v211
	global_store_dwordx4 v3, v[188:191], s[16:17] offset:256
	s_waitcnt vmcnt(11)
	v_add_u32_e32 v193, 0x80000, v192
	v_cvt_f32_ubyte0_e32 v204, v148
	v_cvt_f32_ubyte1_e32 v205, v148
	v_cvt_f32_ubyte2_e32 v206, v148
	v_cvt_f32_ubyte3_e32 v207, v148
	v_cvt_f32_ubyte0_e32 v208, v149
	v_cvt_f32_ubyte1_e32 v209, v149
	v_cvt_f32_ubyte2_e32 v210, v149
	v_cvt_f32_ubyte3_e32 v211, v149
	v_pk_mul_f32 v[204:205], v[204:205], s[88:89] op_sel_hi:[1,0]
	v_pk_mul_f32 v[206:207], v[206:207], s[88:89] op_sel_hi:[1,0]
	v_pk_mul_f32 v[208:209], v[208:209], s[88:89] op_sel_hi:[1,0]
	v_pk_mul_f32 v[210:211], v[210:211], s[88:89] op_sel_hi:[1,0]
	v_pk_mul_f32 v[204:205], v[64:65], v[204:205]
	v_pk_mul_f32 v[206:207], v[66:67], v[206:207]
	v_pk_mul_f32 v[208:209], v[60:61], v[208:209]
	v_pk_mul_f32 v[210:211], v[62:63], v[210:211]
	v_cvt_pk_bf16_f32 v176, v204, v205
	v_cvt_pk_bf16_f32 v177, v206, v207
	v_cvt_pk_bf16_f32 v178, v208, v209
	v_cvt_pk_bf16_f32 v179, v210, v211
	global_store_dwordx4 v193, v[176:179], s[16:17]
	v_cvt_f32_ubyte0_e32 v204, v150
	v_cvt_f32_ubyte1_e32 v205, v150
	v_cvt_f32_ubyte2_e32 v206, v150
	v_cvt_f32_ubyte3_e32 v207, v150
	v_cvt_f32_ubyte0_e32 v208, v151
	v_cvt_f32_ubyte1_e32 v209, v151
	v_cvt_f32_ubyte2_e32 v210, v151
	v_cvt_f32_ubyte3_e32 v211, v151
	v_pk_mul_f32 v[204:205], v[204:205], s[88:89] op_sel_hi:[1,0]
	v_pk_mul_f32 v[206:207], v[206:207], s[88:89] op_sel_hi:[1,0]
	v_pk_mul_f32 v[208:209], v[208:209], s[88:89] op_sel_hi:[1,0]
	v_pk_mul_f32 v[210:211], v[210:211], s[88:89] op_sel_hi:[1,0]
	v_pk_mul_f32 v[204:205], v[32:33], v[204:205]
	v_pk_mul_f32 v[206:207], v[34:35], v[206:207]
	v_pk_mul_f32 v[208:209], v[28:29], v[208:209]
	v_pk_mul_f32 v[210:211], v[30:31], v[210:211]
	v_cvt_pk_bf16_f32 v180, v204, v205
	v_cvt_pk_bf16_f32 v181, v206, v207
	v_cvt_pk_bf16_f32 v182, v208, v209
	v_cvt_pk_bf16_f32 v183, v210, v211
	global_store_dwordx4 v193, v[180:183], s[16:17] offset:256
	s_waitcnt vmcnt(12)
	v_add_u32_e32 v3, 0x90000, v192
	v_cvt_f32_ubyte0_e32 v204, v152
	v_cvt_f32_ubyte1_e32 v205, v152
	v_cvt_f32_ubyte2_e32 v206, v152
	v_cvt_f32_ubyte3_e32 v207, v152
	v_cvt_f32_ubyte0_e32 v208, v153
	v_cvt_f32_ubyte1_e32 v209, v153
	v_cvt_f32_ubyte2_e32 v210, v153
	v_cvt_f32_ubyte3_e32 v211, v153
	v_pk_mul_f32 v[204:205], v[204:205], s[88:89] op_sel_hi:[1,0]
	v_pk_mul_f32 v[206:207], v[206:207], s[88:89] op_sel_hi:[1,0]
	v_pk_mul_f32 v[208:209], v[208:209], s[88:89] op_sel_hi:[1,0]
	v_pk_mul_f32 v[210:211], v[210:211], s[88:89] op_sel_hi:[1,0]
	v_pk_mul_f32 v[204:205], v[56:57], v[204:205]
	v_pk_mul_f32 v[206:207], v[58:59], v[206:207]
	v_pk_mul_f32 v[208:209], v[52:53], v[208:209]
	v_pk_mul_f32 v[210:211], v[54:55], v[210:211]
	v_cvt_pk_bf16_f32 v184, v204, v205
	v_cvt_pk_bf16_f32 v185, v206, v207
	v_cvt_pk_bf16_f32 v186, v208, v209
	v_cvt_pk_bf16_f32 v187, v210, v211
	global_store_dwordx4 v3, v[184:187], s[16:17]
	v_cvt_f32_ubyte0_e32 v204, v154
	v_cvt_f32_ubyte1_e32 v205, v154
	v_cvt_f32_ubyte2_e32 v206, v154
	v_cvt_f32_ubyte3_e32 v207, v154
	v_cvt_f32_ubyte0_e32 v208, v155
	v_cvt_f32_ubyte1_e32 v209, v155
	v_cvt_f32_ubyte2_e32 v210, v155
	v_cvt_f32_ubyte3_e32 v211, v155
	v_pk_mul_f32 v[204:205], v[204:205], s[88:89] op_sel_hi:[1,0]
	v_pk_mul_f32 v[206:207], v[206:207], s[88:89] op_sel_hi:[1,0]
	v_pk_mul_f32 v[208:209], v[208:209], s[88:89] op_sel_hi:[1,0]
	v_pk_mul_f32 v[210:211], v[210:211], s[88:89] op_sel_hi:[1,0]
	v_pk_mul_f32 v[204:205], v[24:25], v[204:205]
	v_pk_mul_f32 v[206:207], v[26:27], v[206:207]
	v_pk_mul_f32 v[208:209], v[20:21], v[208:209]
	v_pk_mul_f32 v[210:211], v[22:23], v[210:211]
	v_cvt_pk_bf16_f32 v188, v204, v205
	v_cvt_pk_bf16_f32 v189, v206, v207
	v_cvt_pk_bf16_f32 v190, v208, v209
	v_cvt_pk_bf16_f32 v191, v210, v211
	global_store_dwordx4 v3, v[188:191], s[16:17] offset:256
	s_waitcnt vmcnt(13)
	v_add_u32_e32 v193, 0xa0000, v192
	v_cvt_f32_ubyte0_e32 v204, v156
	v_cvt_f32_ubyte1_e32 v205, v156
	v_cvt_f32_ubyte2_e32 v206, v156
	v_cvt_f32_ubyte3_e32 v207, v156
	v_cvt_f32_ubyte0_e32 v208, v157
	v_cvt_f32_ubyte1_e32 v209, v157
	v_cvt_f32_ubyte2_e32 v210, v157
	v_cvt_f32_ubyte3_e32 v211, v157
	v_pk_mul_f32 v[204:205], v[204:205], s[88:89] op_sel_hi:[1,0]
	v_pk_mul_f32 v[206:207], v[206:207], s[88:89] op_sel_hi:[1,0]
	v_pk_mul_f32 v[208:209], v[208:209], s[88:89] op_sel_hi:[1,0]
	v_pk_mul_f32 v[210:211], v[210:211], s[88:89] op_sel_hi:[1,0]
	v_pk_mul_f32 v[204:205], v[48:49], v[204:205]
	v_pk_mul_f32 v[206:207], v[50:51], v[206:207]
	v_pk_mul_f32 v[208:209], v[44:45], v[208:209]
	v_pk_mul_f32 v[210:211], v[46:47], v[210:211]
	v_cvt_pk_bf16_f32 v176, v204, v205
	v_cvt_pk_bf16_f32 v177, v206, v207
	v_cvt_pk_bf16_f32 v178, v208, v209
	v_cvt_pk_bf16_f32 v179, v210, v211
	global_store_dwordx4 v193, v[176:179], s[16:17]
	v_cvt_f32_ubyte0_e32 v204, v158
	v_cvt_f32_ubyte1_e32 v205, v158
	v_cvt_f32_ubyte2_e32 v206, v158
	v_cvt_f32_ubyte3_e32 v207, v158
	v_cvt_f32_ubyte0_e32 v208, v159
	v_cvt_f32_ubyte1_e32 v209, v159
	v_cvt_f32_ubyte2_e32 v210, v159
	v_cvt_f32_ubyte3_e32 v211, v159
	v_pk_mul_f32 v[204:205], v[204:205], s[88:89] op_sel_hi:[1,0]
	v_pk_mul_f32 v[206:207], v[206:207], s[88:89] op_sel_hi:[1,0]
	v_pk_mul_f32 v[208:209], v[208:209], s[88:89] op_sel_hi:[1,0]
	v_pk_mul_f32 v[210:211], v[210:211], s[88:89] op_sel_hi:[1,0]
	v_pk_mul_f32 v[204:205], v[16:17], v[204:205]
	v_pk_mul_f32 v[206:207], v[18:19], v[206:207]
	v_pk_mul_f32 v[208:209], v[12:13], v[208:209]
	v_pk_mul_f32 v[210:211], v[14:15], v[210:211]
	v_cvt_pk_bf16_f32 v180, v204, v205
	v_cvt_pk_bf16_f32 v181, v206, v207
	v_cvt_pk_bf16_f32 v182, v208, v209
	v_cvt_pk_bf16_f32 v183, v210, v211
	global_store_dwordx4 v193, v[180:183], s[16:17] offset:256
	s_waitcnt vmcnt(14)
	v_add_u32_e32 v3, 0xb0000, v192
	v_cvt_f32_ubyte0_e32 v204, v160
	v_cvt_f32_ubyte1_e32 v205, v160
	v_cvt_f32_ubyte2_e32 v206, v160
	v_cvt_f32_ubyte3_e32 v207, v160
	v_cvt_f32_ubyte0_e32 v208, v161
	v_cvt_f32_ubyte1_e32 v209, v161
	v_cvt_f32_ubyte2_e32 v210, v161
	v_cvt_f32_ubyte3_e32 v211, v161
	v_pk_mul_f32 v[204:205], v[204:205], s[88:89] op_sel_hi:[1,0]
	v_pk_mul_f32 v[206:207], v[206:207], s[88:89] op_sel_hi:[1,0]
	v_pk_mul_f32 v[208:209], v[208:209], s[88:89] op_sel_hi:[1,0]
	v_pk_mul_f32 v[210:211], v[210:211], s[88:89] op_sel_hi:[1,0]
	v_pk_mul_f32 v[204:205], v[40:41], v[204:205]
	v_pk_mul_f32 v[206:207], v[42:43], v[206:207]
	v_pk_mul_f32 v[208:209], v[36:37], v[208:209]
	v_pk_mul_f32 v[210:211], v[38:39], v[210:211]
	v_cvt_pk_bf16_f32 v184, v204, v205
	v_cvt_pk_bf16_f32 v185, v206, v207
	v_cvt_pk_bf16_f32 v186, v208, v209
	v_cvt_pk_bf16_f32 v187, v210, v211
	global_store_dwordx4 v3, v[184:187], s[16:17]
	v_cvt_f32_ubyte0_e32 v204, v162
	v_cvt_f32_ubyte1_e32 v205, v162
	v_cvt_f32_ubyte2_e32 v206, v162
	v_cvt_f32_ubyte3_e32 v207, v162
	v_cvt_f32_ubyte0_e32 v208, v163
	v_cvt_f32_ubyte1_e32 v209, v163
	v_cvt_f32_ubyte2_e32 v210, v163
	v_cvt_f32_ubyte3_e32 v211, v163
	v_pk_mul_f32 v[204:205], v[204:205], s[88:89] op_sel_hi:[1,0]
	v_pk_mul_f32 v[206:207], v[206:207], s[88:89] op_sel_hi:[1,0]
	v_pk_mul_f32 v[208:209], v[208:209], s[88:89] op_sel_hi:[1,0]
	v_pk_mul_f32 v[210:211], v[210:211], s[88:89] op_sel_hi:[1,0]
	v_pk_mul_f32 v[204:205], v[8:9], v[204:205]
	v_pk_mul_f32 v[206:207], v[10:11], v[206:207]
	v_pk_mul_f32 v[208:209], v[4:5], v[208:209]
	v_pk_mul_f32 v[210:211], v[6:7], v[210:211]
	v_cvt_pk_bf16_f32 v188, v204, v205
	v_cvt_pk_bf16_f32 v189, v206, v207
	v_cvt_pk_bf16_f32 v190, v208, v209
	v_cvt_pk_bf16_f32 v191, v210, v211
	global_store_dwordx4 v3, v[188:191], s[16:17] offset:256
	s_mov_b64 s[6:7], 0
.Lbr_done:
.LBB0_475:
	s_andn2_b64 vcc, exec, s[24:25]
	s_mov_b64 s[4:5], -1
	s_cbranch_vccnz .LBB0_379
	s_and_b64 vcc, exec, s[6:7]
	s_cbranch_vccnz .LBB0_478
	v_mov_b32_e32 v2, v1
	v_mov_b32_e32 v3, v1
	v_mov_b32_e32 v0, v1
	v_mov_b64_e32 v[6:7], v[2:3]
	v_mov_b64_e32 v[10:11], v[2:3]
	v_mov_b64_e32 v[14:15], v[2:3]
	v_mov_b64_e32 v[18:19], v[2:3]
	v_mov_b64_e32 v[22:23], v[2:3]
	v_mov_b64_e32 v[26:27], v[2:3]
	v_mov_b64_e32 v[30:31], v[2:3]
	v_mov_b64_e32 v[34:35], v[2:3]
	v_mov_b64_e32 v[38:39], v[2:3]
	v_mov_b64_e32 v[42:43], v[2:3]
	v_mov_b64_e32 v[46:47], v[2:3]
	v_mov_b64_e32 v[50:51], v[2:3]
	v_mov_b64_e32 v[54:55], v[2:3]
	v_mov_b64_e32 v[58:59], v[2:3]
	v_mov_b64_e32 v[62:63], v[2:3]
	v_mov_b64_e32 v[66:67], v[2:3]
	v_mov_b64_e32 v[70:71], v[2:3]
	v_mov_b64_e32 v[74:75], v[2:3]
	v_mov_b64_e32 v[78:79], v[2:3]
	v_mov_b64_e32 v[82:83], v[2:3]
	v_mov_b64_e32 v[86:87], v[2:3]
	v_mov_b64_e32 v[90:91], v[2:3]
	v_mov_b64_e32 v[94:95], v[2:3]
	v_mov_b64_e32 v[98:99], v[2:3]
	v_mov_b64_e32 v[102:103], v[2:3]
	v_mov_b64_e32 v[106:107], v[2:3]
	v_mov_b64_e32 v[110:111], v[2:3]
	v_mov_b64_e32 v[114:115], v[2:3]
	v_mov_b64_e32 v[118:119], v[2:3]
	v_mov_b64_e32 v[122:123], v[2:3]
	v_mov_b64_e32 v[126:127], v[2:3]
	v_mov_b64_e32 v[130:131], v[2:3]
	v_mov_b64_e32 v[4:5], v[0:1]
	v_mov_b64_e32 v[8:9], v[0:1]
	v_mov_b64_e32 v[12:13], v[0:1]
	v_mov_b64_e32 v[16:17], v[0:1]
	v_mov_b64_e32 v[20:21], v[0:1]
	v_mov_b64_e32 v[24:25], v[0:1]
	v_mov_b64_e32 v[28:29], v[0:1]
	v_mov_b64_e32 v[32:33], v[0:1]
	v_mov_b64_e32 v[36:37], v[0:1]
	v_mov_b64_e32 v[40:41], v[0:1]
	v_mov_b64_e32 v[44:45], v[0:1]
	v_mov_b64_e32 v[48:49], v[0:1]
	v_mov_b64_e32 v[52:53], v[0:1]
	v_mov_b64_e32 v[56:57], v[0:1]
	v_mov_b64_e32 v[60:61], v[0:1]
	v_mov_b64_e32 v[64:65], v[0:1]
	v_mov_b64_e32 v[68:69], v[0:1]
	v_mov_b64_e32 v[72:73], v[0:1]
	v_mov_b64_e32 v[76:77], v[0:1]
	v_mov_b64_e32 v[80:81], v[0:1]
	v_mov_b64_e32 v[84:85], v[0:1]
	v_mov_b64_e32 v[88:89], v[0:1]
	v_mov_b64_e32 v[92:93], v[0:1]
	v_mov_b64_e32 v[96:97], v[0:1]
	v_mov_b64_e32 v[100:101], v[0:1]
	v_mov_b64_e32 v[104:105], v[0:1]
	v_mov_b64_e32 v[108:109], v[0:1]
	v_mov_b64_e32 v[112:113], v[0:1]
	v_mov_b64_e32 v[116:117], v[0:1]
	v_mov_b64_e32 v[120:121], v[0:1]
	v_mov_b64_e32 v[124:125], v[0:1]
	v_mov_b64_e32 v[128:129], v[0:1]
